# v109 plus deferred gate/up completion signal (store drain and counter atomic moved behind the next unit's first loads)
# speedup vs baseline: 1.0044x; 1.0044x over previous
; __device__ __forceinline__ int tid_opaque() { int t = threadIdx.x; asm volatile("" : "+v"(t)); return t; }
; __device__ __forceinline__ int vwg_id() { const int G = gridDim.x; return (G % 8 == 0) ? (int)((blockIdx.x % 8) * (G / 8) + blockIdx.x / 8) : (int)blockIdx.x; }
; __device__ __forceinline__ void phase_moe_gu(const Ptrs& p, LAS unsigned char* lds) {
;     const int* counts = (const int*)(p.ws + OFF_CTRL); const bf16_t* h2 = (const bf16_t*)(p.ws + OFF_HA); bf16_t* act = (bf16_t*)(p.ws + OFF_ACT);
;     const __amdgpu_buffer_rsrc_t ract = __builtin_amdgcn_make_buffer_rsrc((void*)act, 0, 0x7ffffff0, 0x00020000);
;     MoeUnit mu; const int cv = counts[tid_opaque() & 31];
;     for (int u = vwg_id(); moe_unit(cv, u, 16, mu); u += gridDim.x) {
;     ...
;         asm volatile("s_waitcnt vmcnt(0)" ::: "memory");
;         __syncthreads();
;         if (threadIdx.x == 0) { __hip_atomic_fetch_add((unsigned*)(p.ws + OFF_GUDONE) + mu.e * 16, 1u, __ATOMIC_RELAXED, __HIP_MEMORY_SCOPE_AGENT);
;                                 __hip_atomic_fetch_add((unsigned*)(p.ws + OFF_GUTOT), 1u, __ATOMIC_RELAXED, __HIP_MEMORY_SCOPE_AGENT); }
.LBB0_1003:
	s_add_u32 s20, s30, 0x18248000
	s_addc_u32 s28, s31, 0
	s_and_b32 s21, s28, 0xffff
	s_mov_b32 s27, 0x20000
	s_mov_b32 s26, 0x7ffffff0
	s_and_b32 s37, s37, 0xffff
	s_movk_i32 s66, 0x6000
	s_mov_b32 s67, 0x80000
	s_mov_b32 s76, 0x82000
	s_mov_b32 s77, 0x84000
	s_mov_b32 s78, 0x86000
	s_mov_b32 s79, 0x88000
	s_mov_b32 s80, 0x8a000
	s_mov_b32 s81, 0x8c000
	s_mov_b32 s82, 0x8e000
	s_movk_i32 s83, 0xf80
	s_add_i32 s29, 0, 0x18000
	s_add_i32 s64, 0, 0x10400
	s_mov_b32 s84, 0xc0e00000
	v_mov_b32_e32 v2, 0
	v_mov_b32_e32 v214, 0x40e00000
	s_mov_b32 s98, 0
	s_waitcnt vmcnt(0)
	v_mov_b32_e32 v247, 0x7fffffff
	s_mov_b32 s1, 0
	v_readlane_b32 s2, v1, 0
	s_add_i32 s2, s2, 0xff
	s_ashr_i32 s2, s2, 8
	s_add_i32 s1, s1, s2
	v_writelane_b32 v247, s1, 0
	v_readlane_b32 s2, v1, 1
	s_add_i32 s2, s2, 0xff
	s_ashr_i32 s2, s2, 8
	s_add_i32 s1, s1, s2
	v_writelane_b32 v247, s1, 1
	v_readlane_b32 s2, v1, 2
	s_add_i32 s2, s2, 0xff
	s_ashr_i32 s2, s2, 8
	s_add_i32 s1, s1, s2
	v_writelane_b32 v247, s1, 2
	v_readlane_b32 s2, v1, 3
	s_add_i32 s2, s2, 0xff
	s_ashr_i32 s2, s2, 8
	s_add_i32 s1, s1, s2
	v_writelane_b32 v247, s1, 3
	v_readlane_b32 s2, v1, 4
	s_add_i32 s2, s2, 0xff
	s_ashr_i32 s2, s2, 8
	s_add_i32 s1, s1, s2
	v_writelane_b32 v247, s1, 4
	v_readlane_b32 s2, v1, 5
	s_add_i32 s2, s2, 0xff
	s_ashr_i32 s2, s2, 8
	s_add_i32 s1, s1, s2
	v_writelane_b32 v247, s1, 5
	v_readlane_b32 s2, v1, 6
	s_add_i32 s2, s2, 0xff
	s_ashr_i32 s2, s2, 8
	s_add_i32 s1, s1, s2
	v_writelane_b32 v247, s1, 6
	v_readlane_b32 s2, v1, 7
	s_add_i32 s2, s2, 0xff
	s_ashr_i32 s2, s2, 8
	s_add_i32 s1, s1, s2
	v_writelane_b32 v247, s1, 7
	v_readlane_b32 s2, v1, 8
	s_add_i32 s2, s2, 0xff
	s_ashr_i32 s2, s2, 8
	s_add_i32 s1, s1, s2
	v_writelane_b32 v247, s1, 8
	v_readlane_b32 s2, v1, 9
	s_add_i32 s2, s2, 0xff
	s_ashr_i32 s2, s2, 8
	s_add_i32 s1, s1, s2
	v_writelane_b32 v247, s1, 9
	v_readlane_b32 s2, v1, 10
	s_add_i32 s2, s2, 0xff
	s_ashr_i32 s2, s2, 8
	s_add_i32 s1, s1, s2
	v_writelane_b32 v247, s1, 10
	v_readlane_b32 s2, v1, 11
	s_add_i32 s2, s2, 0xff
	s_ashr_i32 s2, s2, 8
	s_add_i32 s1, s1, s2
	v_writelane_b32 v247, s1, 11
	v_readlane_b32 s2, v1, 12
	s_add_i32 s2, s2, 0xff
	s_ashr_i32 s2, s2, 8
	s_add_i32 s1, s1, s2
	v_writelane_b32 v247, s1, 12
	v_readlane_b32 s2, v1, 13
	s_add_i32 s2, s2, 0xff
	s_ashr_i32 s2, s2, 8
	s_add_i32 s1, s1, s2
	v_writelane_b32 v247, s1, 13
	v_readlane_b32 s2, v1, 14
	s_add_i32 s2, s2, 0xff
	s_ashr_i32 s2, s2, 8
	s_add_i32 s1, s1, s2
	v_writelane_b32 v247, s1, 14
	v_readlane_b32 s2, v1, 15
	s_add_i32 s2, s2, 0xff
	s_ashr_i32 s2, s2, 8
	s_add_i32 s1, s1, s2
	v_writelane_b32 v247, s1, 15
	v_readlane_b32 s2, v1, 16
	s_add_i32 s2, s2, 0xff
	s_ashr_i32 s2, s2, 8
	s_add_i32 s1, s1, s2
	v_writelane_b32 v247, s1, 16
	v_readlane_b32 s2, v1, 17
	s_add_i32 s2, s2, 0xff
	s_ashr_i32 s2, s2, 8
	s_add_i32 s1, s1, s2
	v_writelane_b32 v247, s1, 17
	v_readlane_b32 s2, v1, 18
	s_add_i32 s2, s2, 0xff
	s_ashr_i32 s2, s2, 8
	s_add_i32 s1, s1, s2
	v_writelane_b32 v247, s1, 18
	v_readlane_b32 s2, v1, 19
	s_add_i32 s2, s2, 0xff
	s_ashr_i32 s2, s2, 8
	s_add_i32 s1, s1, s2
	v_writelane_b32 v247, s1, 19
	v_readlane_b32 s2, v1, 20
	s_add_i32 s2, s2, 0xff
	s_ashr_i32 s2, s2, 8
	s_add_i32 s1, s1, s2
	v_writelane_b32 v247, s1, 20
	v_readlane_b32 s2, v1, 21
	s_add_i32 s2, s2, 0xff
	s_ashr_i32 s2, s2, 8
	s_add_i32 s1, s1, s2
	v_writelane_b32 v247, s1, 21
	v_readlane_b32 s2, v1, 22
	s_add_i32 s2, s2, 0xff
	s_ashr_i32 s2, s2, 8
	s_add_i32 s1, s1, s2
	v_writelane_b32 v247, s1, 22
	v_readlane_b32 s2, v1, 23
	s_add_i32 s2, s2, 0xff
	s_ashr_i32 s2, s2, 8
	s_add_i32 s1, s1, s2
	v_writelane_b32 v247, s1, 23
	v_readlane_b32 s2, v1, 24
	s_add_i32 s2, s2, 0xff
	s_ashr_i32 s2, s2, 8
	s_add_i32 s1, s1, s2
	v_writelane_b32 v247, s1, 24
	v_readlane_b32 s2, v1, 25
	s_add_i32 s2, s2, 0xff
	s_ashr_i32 s2, s2, 8
	s_add_i32 s1, s1, s2
	v_writelane_b32 v247, s1, 25
	v_readlane_b32 s2, v1, 26
	s_add_i32 s2, s2, 0xff
	s_ashr_i32 s2, s2, 8
	s_add_i32 s1, s1, s2
	v_writelane_b32 v247, s1, 26
	v_readlane_b32 s2, v1, 27
	s_add_i32 s2, s2, 0xff
	s_ashr_i32 s2, s2, 8
	s_add_i32 s1, s1, s2
	v_writelane_b32 v247, s1, 27
	v_readlane_b32 s2, v1, 28
	s_add_i32 s2, s2, 0xff
	s_ashr_i32 s2, s2, 8
	s_add_i32 s1, s1, s2
	v_writelane_b32 v247, s1, 28
	v_readlane_b32 s2, v1, 29
	s_add_i32 s2, s2, 0xff
	s_ashr_i32 s2, s2, 8
	s_add_i32 s1, s1, s2
	v_writelane_b32 v247, s1, 29
	v_readlane_b32 s2, v1, 30
	s_add_i32 s2, s2, 0xff
	s_ashr_i32 s2, s2, 8
	s_add_i32 s1, s1, s2
	v_writelane_b32 v247, s1, 30
	v_readlane_b32 s2, v1, 31
	s_add_i32 s2, s2, 0xff
	s_ashr_i32 s2, s2, 8
	s_add_i32 s1, s1, s2
	v_writelane_b32 v247, s1, 31
	s_branch .LBB0_1006
